# tile/token slot taken from the block id so that the two workgroups of a CU (bid, bid+256) get adjacent slots: they stream the same A panel in every tiled phase (L1 reuse)
# speedup vs baseline: 1.0373x; 1.0010x over previous
.LBB0_359:
	s_or_b64 exec, exec, s[0:1]
	s_waitcnt lgkmcnt(0)
	s_barrier
	s_mov_b64 s[2:3], exec
	v_readlane_b32 s0, v253, 10
	v_readlane_b32 s1, v253, 11
	s_and_b64 s[0:1], s[2:3], s[0:1]
	s_mov_b64 exec, s[0:1]
	s_cbranch_execz .LBB0_361
	v_readlane_b32 s4, v254, 22
	v_mov_b32_e32 v1, 0
	v_readlane_b32 s5, v254, 23
	s_getreg_b32 s0, hwreg(HW_REG_XCC_ID, 0, 4)
	s_and_b32 s31, s0, 15
	s_cmp_lg_u32 s31, 0
	s_cselect_b64 vcc, -1, 0
	s_cmp_gt_u32 s31, 1
	global_load_dword v2, v1, s[4:5] sc1
	v_readlane_b32 s4, v254, 24
	v_readlane_b32 s5, v254, 25
	s_load_dword s30, s[94:95], 0x0
	s_cselect_b64 s[0:1], -1, 0
	s_cmp_gt_u32 s31, 2
	s_waitcnt vmcnt(0)
	v_cndmask_b32_e32 v17, 0, v2, vcc
	global_load_dword v3, v1, s[4:5] sc1
	v_readlane_b32 s4, v254, 26
	v_readlane_b32 s5, v254, 27
	v_lshlrev_b32_e32 v2, 3, v2
	s_waitcnt vmcnt(0)
	v_cndmask_b32_e64 v18, 0, v3, s[0:1]
	s_nop 1
	global_load_dword v4, v1, s[4:5] sc1
	v_readlane_b32 s4, v254, 28
	v_readlane_b32 s5, v254, 29
	v_lshlrev_b32_e32 v3, 3, v3
	s_waitcnt lgkmcnt(0)
	v_cmp_eq_u32_e64 s[0:1], s30, v3
	s_nop 1
	global_load_dword v5, v1, s[4:5] sc1
	v_readlane_b32 s4, v254, 30
	v_readlane_b32 s5, v254, 31
	s_nop 4
	global_load_dword v6, v1, s[4:5] sc1
	v_readlane_b32 s4, v254, 32
	v_readlane_b32 s5, v254, 33
	s_nop 4
	global_load_dword v7, v1, s[4:5] sc1
	v_readlane_b32 s4, v254, 34
	v_readlane_b32 s5, v254, 35
	s_nop 4
	global_load_dword v8, v1, s[4:5] sc1
	v_readlane_b32 s4, v254, 36
	v_readlane_b32 s5, v254, 37
	s_nop 4
	global_load_dword v9, v1, s[4:5] sc1
	v_readlane_b32 s4, v254, 38
	v_readlane_b32 s5, v254, 39
	s_nop 4
	global_load_dword v10, v1, s[4:5] sc1
	v_readlane_b32 s4, v254, 40
	v_readlane_b32 s5, v254, 41
	s_nop 4
	global_load_dword v11, v1, s[4:5] sc1
	v_readlane_b32 s4, v254, 42
	v_readlane_b32 s5, v254, 43
	s_nop 4
	global_load_dword v12, v1, s[4:5] sc1
	v_readlane_b32 s4, v254, 44
	v_readlane_b32 s5, v254, 45
	s_nop 4
	global_load_dword v13, v1, s[4:5] sc1
	v_readlane_b32 s4, v254, 46
	v_readlane_b32 s5, v254, 47
	s_nop 4
	global_load_dword v14, v1, s[4:5] sc1
	v_readlane_b32 s4, v254, 48
	v_readlane_b32 s5, v254, 49
	s_nop 4
	global_load_dword v15, v1, s[4:5] sc1
	v_readlane_b32 s4, v254, 50
	v_readlane_b32 s5, v254, 51
	s_nop 4
	global_load_dword v16, v1, s[4:5] sc1
	v_readlane_b32 s4, v254, 52
	v_readlane_b32 s5, v254, 53
	s_nop 4
	global_load_dword v1, v1, s[4:5] sc1
	s_cselect_b64 s[4:5], -1, 0
	s_cmp_gt_u32 s31, 3
	s_cselect_b64 s[6:7], -1, 0
	s_cmp_gt_u32 s31, 4
	s_cselect_b64 s[8:9], -1, 0
	s_cmp_gt_u32 s31, 5
	s_cselect_b64 s[10:11], -1, 0
	s_cmp_gt_u32 s31, 6
	s_cselect_b64 s[14:15], -1, 0
	s_cmp_gt_u32 s31, 7
	s_cselect_b64 s[16:17], -1, 0
	s_cmp_gt_u32 s31, 8
	s_cselect_b64 s[18:19], -1, 0
	s_cmp_gt_u32 s31, 9
	s_cselect_b64 s[20:21], -1, 0
	s_cmp_gt_u32 s31, 10
	s_cselect_b64 s[22:23], -1, 0
	s_cmp_gt_u32 s31, 11
	s_cselect_b64 s[24:25], -1, 0
	s_cmp_gt_u32 s31, 12
	s_cselect_b64 s[26:27], -1, 0
	s_cmp_gt_u32 s31, 13
	s_cselect_b64 s[28:29], -1, 0
	s_cmp_eq_u32 s31, 15
	s_cselect_b64 vcc, -1, 0
	s_waitcnt vmcnt(13)
	v_cndmask_b32_e64 v19, 0, v4, s[4:5]
	s_waitcnt vmcnt(12)
	v_cndmask_b32_e64 v20, 0, v5, s[6:7]
	s_waitcnt vmcnt(8)
	v_cndmask_b32_e64 v24, 0, v9, s[16:17]
	v_lshlrev_b32_e32 v9, 3, v9
	v_cndmask_b32_e64 v21, 0, v6, s[8:9]
	v_cndmask_b32_e64 v23, 0, v8, s[14:15]
	v_lshlrev_b32_e32 v8, 3, v8
	s_waitcnt vmcnt(7)
	v_cndmask_b32_e64 v25, 0, v10, s[18:19]
	v_cmp_eq_u32_e64 s[16:17], s30, v9
	v_cndmask_b32_e64 v22, 0, v7, s[10:11]
	v_lshlrev_b32_e32 v7, 3, v7
	v_cmp_eq_u32_e64 s[14:15], s30, v8
	v_lshlrev_b32_e32 v6, 3, v6
	v_cmp_eq_u32_e64 s[10:11], s30, v7
	v_lshlrev_b32_e32 v5, 3, v5
	v_cmp_eq_u32_e64 s[8:9], s30, v6
	v_cmp_eq_u32_e64 s[6:7], s30, v5
	s_waitcnt vmcnt(6)
	v_cndmask_b32_e64 v26, 0, v11, s[20:21]
	v_lshlrev_b32_e32 v4, 3, v4
	s_waitcnt vmcnt(5)
	v_cndmask_b32_e64 v27, 0, v12, s[22:23]
	v_cmp_eq_u32_e64 s[4:5], s30, v4
	s_waitcnt vmcnt(4)
	v_cndmask_b32_e64 v28, 0, v13, s[24:25]
	s_waitcnt vmcnt(3)
	v_cndmask_b32_e64 v29, 0, v14, s[26:27]
	s_waitcnt vmcnt(2)
	v_cndmask_b32_e64 v30, 0, v15, s[28:29]
	s_waitcnt vmcnt(1)
	v_cndmask_b32_e32 v31, 0, v16, vcc
	v_cmp_eq_u32_e32 vcc, s30, v2
	v_add_u32_e32 v2, v18, v17
	v_add_u32_e32 v2, v19, v2
	v_add_u32_e32 v2, v20, v2
	v_add_u32_e32 v2, v21, v2
	v_add_u32_e32 v2, v22, v2
	v_add_u32_e32 v2, v23, v2
	s_waitcnt vmcnt(0)
	v_or_b32_e32 v1, v1, v16
	v_or_b32_e32 v1, v1, v15
	v_or_b32_e32 v1, v1, v14
	v_or_b32_e32 v1, v1, v13
	v_or_b32_e32 v1, v1, v12
	v_or_b32_e32 v1, v1, v11
	v_or_b32_e32 v1, v1, v10
	v_cmp_eq_u32_e64 s[18:19], 0, v1
	s_and_b64 s[16:17], s[18:19], s[16:17]
	s_and_b64 s[14:15], s[16:17], s[14:15]
	s_and_b64 s[10:11], s[14:15], s[10:11]
	v_add_u32_e32 v2, v24, v2
	s_and_b64 s[8:9], s[10:11], s[8:9]
	v_add_u32_e32 v2, v25, v2
	s_and_b64 s[6:7], s[8:9], s[6:7]
	s_add_i32 s8, 0, 0x123e8
	v_add_u32_e32 v2, v26, v2
	v_mov_b32_e32 v1, s8
	v_add_u32_e32 v2, v27, v2
	ds_read_b32 v1, v1
	v_add_u32_e32 v2, v28, v2
	s_and_b64 s[4:5], s[6:7], s[4:5]
	v_add_u32_e32 v2, v29, v2
	s_and_b64 s[0:1], s[4:5], s[0:1]
	v_add_u32_e32 v2, v30, v2
	s_and_b64 s[0:1], s[0:1], vcc
	v_add_u32_e32 v2, v31, v2
	v_cndmask_b32_e64 v3, 0, 1, s[0:1]
	s_add_i32 s0, 0, 0x123ec
	s_waitcnt lgkmcnt(0)
	v_add_u32_e32 v1, v1, v2
	v_mov_b32_e32 v2, s0
	s_add_i32 s0, 0, 0x123f4
	s_and_b32 s4, s90, 7
	s_lshl_b32 s4, s4, 6
	s_bfe_u32 s5, s90, 0x50003
	s_lshl_b32 s5, s5, 1
	s_lshr_b32 s6, s90, 8
	s_add_i32 s4, s4, s5
	s_add_i32 s4, s4, s6
	v_mov_b32_e32 v1, s4
	ds_write_b32 v2, v1
	v_mov_b32_e32 v1, s0
	ds_write_b32 v1, v3
